# v11 + scan o-store pairing + GLA-pre q/k staged reads hoisted + out-proj residual epilogue (in-place path): all 16 residual loads up front as global loads, counted waits instead of full drains
# baseline (speedup 1.0000x reference)
.LBB0_410:
	s_or_b64 exec, exec, s[2:3]
	v_add_u32_e32 v5, s17, v55
	v_add3_u32 v21, v5, v56, v54
	v_add_u32_e32 v160, 0xe000, v21
	ds_read_u16 v128, v21 offset:57344
	ds_read_u16 v129, v21 offset:57600
	ds_read_u16 v130, v160 offset:16384
	ds_read_u16 v131, v160 offset:16640
	ds_read_u16 v132, v21 offset:57856
	ds_read_u16 v133, v21 offset:58112
	ds_read_u16 v134, v160 offset:16896
	ds_read_u16 v135, v160 offset:17152
	ds_read_u16 v136, v21 offset:61440
	ds_read_u16 v137, v21 offset:61696
	ds_read_u16 v138, v160 offset:20480
	ds_read_u16 v139, v160 offset:20736
	ds_read_u16 v140, v21 offset:61952
	ds_read_u16 v141, v21 offset:62208
	ds_read_u16 v142, v160 offset:20992
	ds_read_u16 v143, v160 offset:21248
	ds_read_u16 v144, v160 offset:8192
	ds_read_u16 v145, v160 offset:8448
	ds_read_u16 v146, v160 offset:24576
	ds_read_u16 v147, v160 offset:24832
	ds_read_u16 v148, v160 offset:8704
	ds_read_u16 v149, v160 offset:8960
	ds_read_u16 v150, v160 offset:25088
	ds_read_u16 v151, v160 offset:25344
	ds_read_u16 v152, v160 offset:12288
	ds_read_u16 v153, v160 offset:12544
	ds_read_u16 v154, v160 offset:28672
	ds_read_u16 v155, v160 offset:28928
	ds_read_u16 v156, v160 offset:12800
	ds_read_u16 v157, v160 offset:13056
	ds_read_u16 v158, v160 offset:29184
	ds_read_u16 v159, v160 offset:29440
	s_and_b32 s2, s95, 3
	s_mul_i32 s2, s2, 17
	s_ashr_i32 s3, s95, 8
	v_exp_f32_e32 v28, v44
	v_exp_f32_e32 v29, v45
	s_add_i32 s2, s2, s3
	s_mulk_i32 s96, 0x44
	s_add_i32 s16, s2, s96
	s_waitcnt lgkmcnt(15)
	v_lshlrev_b32_e32 v33, 16, v129
	v_lshlrev_b32_e32 v32, 16, v128
	s_mov_b32 s2, 0x3db504f3
	v_pk_mul_f32 v[32:33], v[32:33], s[2:3] op_sel_hi:[1,0]
	v_exp_f32_e32 v20, v30
	v_add_u32_e32 v5, 0xe000, v21
	v_rcp_f32_e32 v30, v28
	v_rcp_f32_e32 v31, v29
	v_pk_mul_f32 v[28:29], v[28:29], v[32:33]
	v_exp_f32_e32 v26, v26
	v_cvt_pk_bf16_f32 v36, v28, v29
	v_exp_f32_e32 v27, v27
	v_exp_f32_e32 v24, v24
	v_exp_f32_e32 v25, v25
	s_waitcnt lgkmcnt(15)
	v_lshlrev_b32_e32 v28, 16, v130
	v_lshlrev_b32_e32 v29, 16, v131
	v_pk_mul_f32 v[32:33], v[30:31], v[28:29]
	v_pk_mul_f32 v[30:31], v[20:21], v[30:31] op_sel_hi:[0,1]
	v_cvt_pk_bf16_f32 v32, v32, v33
	v_add_u32_e32 v33, v57, v60
	ds_write_b16 v33, v36
	ds_write_b16_d16_hi v70, v36
	ds_write_b16 v33, v32 offset:16384
	ds_write_b16_d16_hi v70, v32 offset:16384
	v_pk_mul_f32 v[28:29], v[30:31], v[28:29]
	v_exp_f32_e32 v30, v34
	v_cvt_pk_bf16_f32 v28, v28, v29
	v_exp_f32_e32 v31, v35
	v_rcp_f32_e32 v32, v30
	v_exp_f32_e32 v22, v22
	v_exp_f32_e32 v23, v23
	s_waitcnt lgkmcnt(15)
	v_lshlrev_b32_e32 v35, 16, v133
	v_lshlrev_b32_e32 v34, 16, v132
	v_pk_mul_f32 v[34:35], v[34:35], s[2:3] op_sel_hi:[1,0]
	v_rcp_f32_e32 v33, v31
	v_pk_mul_f32 v[30:31], v[30:31], v[34:35]
	v_exp_f32_e32 v18, v18
	v_cvt_pk_bf16_f32 v29, v30, v31
	v_exp_f32_e32 v19, v19
	v_exp_f32_e32 v16, v16
	v_exp_f32_e32 v17, v17
	s_waitcnt lgkmcnt(15)
	v_lshlrev_b32_e32 v30, 16, v134
	v_lshlrev_b32_e32 v31, 16, v135
	v_pk_mul_f32 v[34:35], v[32:33], v[30:31]
	v_pk_mul_f32 v[32:33], v[20:21], v[32:33] op_sel_hi:[0,1]
	v_pk_mul_f32 v[30:31], v[32:33], v[30:31]
	v_cvt_pk_bf16_f32 v34, v34, v35
	ds_write_b16 v71, v29
	ds_write_b16_d16_hi v72, v29
	ds_write_b16 v71, v34 offset:16384
	ds_write_b16_d16_hi v72, v34 offset:16384
	v_cvt_pk_bf16_f32 v29, v30, v31
	ds_write_b64 v73, v[28:29] offset:32768
	v_rcp_f32_e32 v28, v26
	v_rcp_f32_e32 v29, v27
	v_exp_f32_e32 v6, v6
	s_waitcnt lgkmcnt(15)
	v_lshlrev_b32_e32 v30, 16, v136
	v_lshlrev_b32_e32 v31, 16, v137
	v_pk_mul_f32 v[30:31], v[30:31], s[2:3] op_sel_hi:[1,0]
	v_exp_f32_e32 v7, v7
	v_pk_mul_f32 v[26:27], v[26:27], v[30:31]
	s_ashr_i32 s17, s16, 31
	v_cvt_pk_bf16_f32 v32, v26, v27
	s_movk_i32 s10, 0x2000
	s_waitcnt lgkmcnt(15)
	v_lshlrev_b32_e32 v26, 16, v138
	v_lshlrev_b32_e32 v27, 16, v139
	v_pk_mul_f32 v[30:31], v[28:29], v[26:27]
	v_pk_mul_f32 v[28:29], v[20:21], v[28:29] op_sel_hi:[0,1]
	v_cvt_pk_bf16_f32 v30, v30, v31
	ds_write_b16 v74, v32
	ds_write_b16_d16_hi v75, v32
	ds_write_b16 v74, v30 offset:16384
	ds_write_b16_d16_hi v75, v30 offset:16384
	v_pk_mul_f32 v[26:27], v[28:29], v[26:27]
	v_rcp_f32_e32 v28, v24
	v_cvt_pk_bf16_f32 v26, v26, v27
	v_rcp_f32_e32 v29, v25
	s_waitcnt lgkmcnt(15)
	v_lshlrev_b32_e32 v30, 16, v140
	v_lshlrev_b32_e32 v31, 16, v141
	v_pk_mul_f32 v[30:31], v[30:31], s[2:3] op_sel_hi:[1,0]
	s_nop 0
	v_pk_mul_f32 v[24:25], v[24:25], v[30:31]
	s_nop 0
	v_cvt_pk_bf16_f32 v21, v24, v25
	s_waitcnt lgkmcnt(15)
	v_lshlrev_b32_e32 v24, 16, v142
	v_lshlrev_b32_e32 v25, 16, v143
	v_pk_mul_f32 v[30:31], v[28:29], v[24:25]
	v_pk_mul_f32 v[28:29], v[20:21], v[28:29] op_sel_hi:[0,1]
	v_cvt_pk_bf16_f32 v27, v30, v31
	v_pk_mul_f32 v[24:25], v[28:29], v[24:25]
	ds_write_b16 v76, v21
	ds_write_b16_d16_hi v77, v21
	ds_write_b16 v76, v27 offset:16384
	ds_write_b16_d16_hi v77, v27 offset:16384
	v_cvt_pk_bf16_f32 v27, v24, v25
	ds_write_b64 v78, v[26:27] offset:32768
	v_rcp_f32_e32 v24, v22
	v_rcp_f32_e32 v25, v23
	s_waitcnt lgkmcnt(15)
	v_lshlrev_b32_e32 v27, 16, v145
	v_lshlrev_b32_e32 v26, 16, v144
	v_pk_mul_f32 v[26:27], v[26:27], s[2:3] op_sel_hi:[1,0]
	s_nop 0
	v_pk_mul_f32 v[22:23], v[22:23], v[26:27]
	s_nop 0
	v_cvt_pk_bf16_f32 v21, v22, v23
	s_waitcnt lgkmcnt(15)
	v_lshlrev_b32_e32 v22, 16, v146
	v_lshlrev_b32_e32 v23, 16, v147
	v_pk_mul_f32 v[26:27], v[24:25], v[22:23]
	v_pk_mul_f32 v[24:25], v[20:21], v[24:25] op_sel_hi:[0,1]
	v_cvt_pk_bf16_f32 v26, v26, v27
	ds_write_b16 v79, v21
	ds_write_b16_d16_hi v80, v21
	ds_write_b16 v79, v26 offset:16384
	ds_write_b16_d16_hi v80, v26 offset:16384
	v_pk_mul_f32 v[22:23], v[24:25], v[22:23]
	v_rcp_f32_e32 v24, v18
	v_cvt_pk_bf16_f32 v22, v22, v23
	v_rcp_f32_e32 v25, v19
	s_waitcnt lgkmcnt(15)
	v_lshlrev_b32_e32 v26, 16, v148
	v_lshlrev_b32_e32 v27, 16, v149
	v_pk_mul_f32 v[26:27], v[26:27], s[2:3] op_sel_hi:[1,0]
	s_nop 0
	v_pk_mul_f32 v[18:19], v[18:19], v[26:27]
	s_nop 0
	v_cvt_pk_bf16_f32 v21, v18, v19
	s_waitcnt lgkmcnt(15)
	v_lshlrev_b32_e32 v18, 16, v150
	v_lshlrev_b32_e32 v19, 16, v151
	v_pk_mul_f32 v[26:27], v[24:25], v[18:19]
	v_pk_mul_f32 v[24:25], v[20:21], v[24:25] op_sel_hi:[0,1]
	v_cvt_pk_bf16_f32 v23, v26, v27
	v_pk_mul_f32 v[18:19], v[24:25], v[18:19]
	ds_write_b16 v81, v21
	ds_write_b16_d16_hi v82, v21
	ds_write_b16 v81, v23 offset:16384
	ds_write_b16_d16_hi v82, v23 offset:16384
	v_cvt_pk_bf16_f32 v23, v18, v19
	ds_write_b64 v83, v[22:23] offset:32768
	v_rcp_f32_e32 v18, v16
	v_rcp_f32_e32 v19, v17
	s_waitcnt lgkmcnt(15)
	v_lshlrev_b32_e32 v23, 16, v153
	v_lshlrev_b32_e32 v22, 16, v152
	v_pk_mul_f32 v[22:23], v[22:23], s[2:3] op_sel_hi:[1,0]
	s_nop 0
	v_pk_mul_f32 v[16:17], v[16:17], v[22:23]
	s_nop 0
	v_cvt_pk_bf16_f32 v21, v16, v17
	s_waitcnt lgkmcnt(15)
	v_lshlrev_b32_e32 v16, 16, v154
	v_lshlrev_b32_e32 v17, 16, v155
	v_pk_mul_f32 v[22:23], v[18:19], v[16:17]
	v_pk_mul_f32 v[18:19], v[20:21], v[18:19] op_sel_hi:[0,1]
	v_cvt_pk_bf16_f32 v22, v22, v23
	ds_write_b16 v84, v21
	ds_write_b16_d16_hi v85, v21
	ds_write_b16 v84, v22 offset:16384
	ds_write_b16_d16_hi v85, v22 offset:16384
	v_pk_mul_f32 v[16:17], v[18:19], v[16:17]
	v_rcp_f32_e32 v18, v6
	v_cvt_pk_bf16_f32 v16, v16, v17
	v_rcp_f32_e32 v19, v7
	s_waitcnt lgkmcnt(15)
	v_lshlrev_b32_e32 v22, 16, v156
	v_lshlrev_b32_e32 v23, 16, v157
	v_pk_mul_f32 v[22:23], v[22:23], s[2:3] op_sel_hi:[1,0]
	s_lshl_b64 s[2:3], s[16:17], 14
	v_pk_mul_f32 v[6:7], v[6:7], v[22:23]
	s_nop 0
	v_cvt_pk_bf16_f32 v17, v6, v7
	s_waitcnt lgkmcnt(15)
	v_lshlrev_b32_e32 v6, 16, v158
	v_lshlrev_b32_e32 v7, 16, v159
	v_pk_mul_f32 v[22:23], v[18:19], v[6:7]
	v_pk_mul_f32 v[18:19], v[20:21], v[18:19] op_sel_hi:[0,1]
	v_cvt_pk_bf16_f32 v5, v22, v23
	v_pk_mul_f32 v[6:7], v[18:19], v[6:7]
	ds_write_b16 v86, v17
	ds_write_b16_d16_hi v87, v17
	ds_write_b16 v86, v5 offset:16384
	ds_write_b16_d16_hi v87, v5 offset:16384
	v_cvt_pk_bf16_f32 v17, v6, v7
	v_add_u32_e32 v5, v58, v61
	ds_write_b64 v88, v[16:17] offset:32768
	s_waitcnt lgkmcnt(0)
	s_barrier
	ds_read_b128 v[16:19], v5
	v_add_u32_e32 v5, s81, v62
	ds_read_b128 v[20:23], v5 offset:16384
	v_add_u32_e32 v5, s82, v62
	ds_read_b128 v[24:27], v5 offset:16384
	v_add_u32_e32 v5, v58, v63
	s_waitcnt lgkmcnt(0)
	v_mfma_f32_16x16x32_bf16 v[20:23], v[20:23], v[16:19], 0
	v_cndmask_b32_e64 v6, 0, 1, s[26:27]
	v_cndmask_b32_e64 v7, 0, 1, s[18:19]
	v_mfma_f32_16x16x32_bf16 v[16:19], v[24:27], v[16:19], 0
	ds_read_b128 v[24:27], v5
	v_add_u32_e32 v5, s81, v65
	ds_read_b128 v[28:31], v5 offset:16384
	v_add_u32_e32 v5, s82, v65
	s_waitcnt lgkmcnt(0)
	v_mfma_f32_16x16x32_bf16 v[20:23], v[28:31], v[24:27], v[20:23]
	ds_read_b128 v[28:31], v5 offset:16384
	v_add_u32_e32 v5, v58, v66
	s_waitcnt lgkmcnt(0)
	v_mfma_f32_16x16x32_bf16 v[16:19], v[28:31], v[24:27], v[16:19]
	ds_read_b128 v[24:27], v5
	v_add_u32_e32 v5, s81, v67
	ds_read_b128 v[28:31], v5 offset:16384
	v_add_u32_e32 v5, s82, v67
	s_waitcnt lgkmcnt(0)
	v_mfma_f32_16x16x32_bf16 v[20:23], v[28:31], v[24:27], v[20:23]
	ds_read_b128 v[28:31], v5 offset:16384
	v_add_u32_e32 v5, v58, v68
	s_waitcnt lgkmcnt(0)
	v_mfma_f32_16x16x32_bf16 v[16:19], v[28:31], v[24:27], v[16:19]
	ds_read_b128 v[24:27], v5
	v_add_u32_e32 v5, s81, v69
	ds_read_b128 v[28:31], v5 offset:16384
	v_add_u32_e32 v5, s82, v69
	s_waitcnt lgkmcnt(0)
	v_mfma_f32_16x16x32_bf16 v[20:23], v[28:31], v[24:27], v[20:23]
	ds_read_b128 v[28:31], v5 offset:16384
	v_cndmask_b32_e64 v5, 0, 1, s[74:75]
	v_cndmask_b32_e64 v5, v6, v5, s[72:73]
	v_cndmask_b32_e64 v6, 0, 1, s[20:21]
	v_and_b32_e32 v5, 1, v5
	v_cndmask_b32_e64 v6, v7, v6, s[72:73]
	v_cmp_eq_u32_e32 vcc, 1, v5
	v_and_b32_e32 v6, 1, v6
	v_cndmask_b32_e64 v7, 0, 1, s[24:25]
	v_cndmask_b32_e32 v5, 0, v20, vcc
	v_cmp_eq_u32_e32 vcc, 1, v6
	v_cndmask_b32_e64 v20, 0, 1, s[22:23]
	v_cndmask_b32_e64 v7, v20, v7, s[72:73]
	v_cndmask_b32_e32 v6, 0, v21, vcc
	v_cndmask_b32_e64 v20, 0, 1, s[54:55]
	v_cndmask_b32_e64 v21, 0, 1, s[52:53]
	v_and_b32_e32 v7, 1, v7
	v_cndmask_b32_e64 v20, v21, v20, s[72:73]
	v_cmp_eq_u32_e32 vcc, 1, v7
	v_and_b32_e32 v20, 1, v20
	v_cvt_pk_bf16_f32 v6, v5, v6
	v_cndmask_b32_e32 v7, 0, v22, vcc
	v_cmp_eq_u32_e32 vcc, 1, v20
	s_waitcnt lgkmcnt(0)
	v_mfma_f32_16x16x32_bf16 v[16:19], v[28:31], v[24:27], v[16:19]
	v_cndmask_b32_e64 v5, 0, 1, s[58:59]
	v_cndmask_b32_e32 v20, 0, v23, vcc
	v_cvt_pk_bf16_f32 v7, v7, v20
	ds_write_b64 v89, v[6:7] offset:49152
	v_cndmask_b32_e64 v6, 0, 1, s[56:57]
	v_cndmask_b32_e64 v5, v6, v5, s[72:73]
	v_cndmask_b32_e64 v6, 0, 1, s[62:63]
	v_cndmask_b32_e64 v7, 0, 1, s[60:61]
	v_and_b32_e32 v5, 1, v5
	v_cndmask_b32_e64 v6, v7, v6, s[72:73]
	v_cmp_eq_u32_e32 vcc, 1, v5
	v_and_b32_e32 v6, 1, v6
	v_cndmask_b32_e64 v7, 0, 1, s[66:67]
	v_cndmask_b32_e32 v5, 0, v16, vcc
	v_cmp_eq_u32_e32 vcc, 1, v6
	v_cndmask_b32_e64 v16, 0, 1, s[64:65]
	v_cndmask_b32_e64 v7, v16, v7, s[72:73]
	v_cndmask_b32_e32 v6, 0, v17, vcc
	v_cndmask_b32_e64 v16, 0, 1, s[70:71]
	v_cndmask_b32_e64 v17, 0, 1, s[68:69]
	v_and_b32_e32 v7, 1, v7
	v_cndmask_b32_e64 v16, v17, v16, s[72:73]
	v_cmp_eq_u32_e32 vcc, 1, v7
	v_and_b32_e32 v16, 1, v16
	v_cvt_pk_bf16_f32 v6, v5, v6
	v_cndmask_b32_e32 v7, 0, v18, vcc
	v_cmp_eq_u32_e32 vcc, 1, v16
	v_add_u32_e32 v5, 0, v59
	s_add_u32 s72, s86, s2
	v_cndmask_b32_e32 v16, 0, v19, vcc
	v_cvt_pk_bf16_f32 v7, v7, v16
	ds_write_b64 v90, v[6:7] offset:49152
	s_waitcnt lgkmcnt(0)
	s_barrier
	ds_read_b128 v[16:19], v5
	s_addc_u32 s73, s87, s3
	v_lshlrev_b64 v[6:7], 4, v[12:13]
	v_lshl_add_u64 v[20:21], s[72:73], 0, v[6:7]
	s_add_u32 s96, s88, s2
	s_waitcnt lgkmcnt(0)
	global_store_dwordx4 v[20:21], v[16:19], off
	ds_read_b128 v[16:19], v91
	v_add_co_u32_e32 v20, vcc, s10, v20
	s_addc_u32 s97, s89, s3
	s_nop 0
	v_addc_co_u32_e32 v21, vcc, 0, v21, vcc
	s_waitcnt lgkmcnt(0)
	global_store_dwordx4 v[20:21], v[16:19], off
	ds_read_b128 v[16:19], v5 offset:32768
	v_lshl_add_u64 v[20:21], s[96:97], 0, v[6:7]
	s_lshl_b64 s[2:3], s[16:17], 13
	s_add_u32 s2, s90, s2
	s_addc_u32 s3, s91, s3
	s_waitcnt lgkmcnt(0)
	global_store_dwordx4 v[20:21], v[16:19], off
	ds_read_b128 v[16:19], v91 offset:32768
	v_add_co_u32_e32 v20, vcc, 0x2000, v20
	v_lshl_add_u64 v[6:7], s[2:3], 0, v[6:7]
	s_nop 0
	v_addc_co_u32_e32 v21, vcc, 0, v21, vcc
	s_waitcnt lgkmcnt(0)
	global_store_dwordx4 v[20:21], v[16:19], off
	ds_read_b128 v[16:19], v5 offset:49152
	s_waitcnt lgkmcnt(0)
	global_store_dwordx4 v[6:7], v[16:19], off
	s_and_saveexec_b64 s[2:3], s[76:77]
	s_cbranch_execz .LBB0_393
	v_add_u32_e32 v5, 0x22000, v5
	ds_read_b128 v[16:19], v5
	s_lshl_b64 s[16:17], s[16:17], 9
	s_add_u32 s16, s92, s16
	s_addc_u32 s17, s93, s17
	v_lshl_add_u64 v[6:7], v[12:13], 4, s[16:17]
	s_waitcnt lgkmcnt(0)
	global_store_dwordx4 v[6:7], v[16:19], off
	s_branch .LBB0_393

.LBB0_1118:
	s_mov_b32 s2, 0x40000
	s_nop 0
	global_load_dwordx4 v[174:177], v[188:189], off
	global_load_dwordx4 v[178:181], v[188:189], off offset:256
	v_add_co_u32_e32 v172, vcc, 0x8000, v188
	s_nop 0
	v_addc_co_u32_e32 v173, vcc, 0, v189, vcc
	global_load_dwordx4 v[182:185], v[172:173], off
	global_load_dwordx4 v[164:167], v[172:173], off offset:256
	v_add_co_u32_e32 v170, vcc, 0x10000, v188
	s_nop 0
	v_addc_co_u32_e32 v171, vcc, 0, v189, vcc
	global_load_dwordx4 v[160:163], v[170:171], off
	global_load_dwordx4 v[152:155], v[170:171], off offset:256
	v_add_co_u32_e32 v168, vcc, 0x18000, v188
	s_nop 0
	v_addc_co_u32_e32 v169, vcc, 0, v189, vcc
	global_load_dwordx4 v[156:159], v[168:169], off
	global_load_dwordx4 v[148:151], v[168:169], off offset:256
	v_add_co_u32_e32 v198, vcc, 0x40000, v188
	s_nop 0
	v_addc_co_u32_e32 v199, vcc, 0, v189, vcc
	global_load_dwordx4 v[194:197], v[198:199], off
	global_load_dwordx4 v[198:201], v[198:199], off offset:256
	v_add_co_u32_e32 v210, vcc, 0x48000, v188
	s_nop 0
	v_addc_co_u32_e32 v211, vcc, 0, v189, vcc
	global_load_dwordx4 v[206:209], v[210:211], off
	global_load_dwordx4 v[210:213], v[210:211], off offset:256
	v_add_co_u32_e32 v218, vcc, 0x50000, v188
	s_nop 0
	v_addc_co_u32_e32 v219, vcc, 0, v189, vcc
	global_load_dwordx4 v[214:217], v[218:219], off
	global_load_dwordx4 v[218:221], v[218:219], off offset:256
	v_add_co_u32_e32 v226, vcc, 0x58000, v188
	s_nop 0
	v_addc_co_u32_e32 v227, vcc, 0, v189, vcc
	global_load_dwordx4 v[222:225], v[226:227], off
	global_load_dwordx4 v[226:229], v[226:227], off offset:256
	s_waitcnt vmcnt(12) lgkmcnt(0)
	v_lshlrev_b32_e32 v186, 16, v174
	v_and_b32_e32 v187, 0xffff0000, v174
	s_nop 0
	v_lshlrev_b32_e32 v174, 16, v175
	v_and_b32_e32 v175, 0xffff0000, v175
	v_lshlrev_b32_e32 v190, 16, v176
	v_and_b32_e32 v191, 0xffff0000, v176
	v_lshlrev_b32_e32 v176, 16, v177
	v_and_b32_e32 v177, 0xffff0000, v177
	v_pk_fma_f32 v[142:143], v[142:143], v[46:47], v[174:175]
	v_pk_fma_f32 v[140:141], v[140:141], v[44:45], v[186:187]
	v_pk_fma_f32 v[146:147], v[146:147], v[42:43], v[176:177]
	v_pk_fma_f32 v[144:145], v[144:145], v[40:41], v[190:191]
	v_cvt_pk_bf16_f32 v140, v140, v141
	v_cvt_pk_bf16_f32 v141, v142, v143
	v_cvt_pk_bf16_f32 v142, v144, v145
	v_cvt_pk_bf16_f32 v143, v146, v147
	global_store_dwordx4 v[188:189], v[140:143], off
	v_lshlrev_b32_e32 v144, 16, v180
	v_and_b32_e32 v145, 0xffff0000, v180
	v_lshlrev_b32_e32 v140, 16, v178
	v_and_b32_e32 v141, 0xffff0000, v178
	v_lshlrev_b32_e32 v142, 16, v179
	v_and_b32_e32 v143, 0xffff0000, v179
	v_lshlrev_b32_e32 v146, 16, v181
	v_and_b32_e32 v147, 0xffff0000, v181
	v_pk_fma_f32 v[138:139], v[138:139], v[38:39], v[142:143]
	v_pk_fma_f32 v[136:137], v[136:137], v[36:37], v[140:141]
	v_pk_fma_f32 v[140:141], v[134:135], v[30:31], v[146:147]
	v_pk_fma_f32 v[134:135], v[132:133], v[28:29], v[144:145]
	v_cvt_pk_bf16_f32 v132, v136, v137
	v_cvt_pk_bf16_f32 v133, v138, v139
	v_cvt_pk_bf16_f32 v134, v134, v135
	v_cvt_pk_bf16_f32 v135, v140, v141
	global_store_dwordx4 v[188:189], v[132:135], off offset:256
	v_lshlrev_b32_e32 v136, 16, v184
	v_and_b32_e32 v137, 0xffff0000, v184
	v_lshlrev_b32_e32 v132, 16, v182
	v_and_b32_e32 v133, 0xffff0000, v182
	v_lshlrev_b32_e32 v134, 16, v183
	v_and_b32_e32 v135, 0xffff0000, v183
	v_lshlrev_b32_e32 v138, 16, v185
	v_and_b32_e32 v139, 0xffff0000, v185
	v_pk_fma_f32 v[126:127], v[126:127], v[46:47], v[134:135]
	v_pk_fma_f32 v[124:125], v[124:125], v[44:45], v[132:133]
	v_pk_fma_f32 v[130:131], v[130:131], v[42:43], v[138:139]
	v_pk_fma_f32 v[128:129], v[128:129], v[40:41], v[136:137]
	v_cvt_pk_bf16_f32 v124, v124, v125
	v_cvt_pk_bf16_f32 v125, v126, v127
	v_cvt_pk_bf16_f32 v126, v128, v129
	v_cvt_pk_bf16_f32 v127, v130, v131
	global_store_dwordx4 v[172:173], v[124:127], off
	v_lshlrev_b32_e32 v128, 16, v166
	v_and_b32_e32 v129, 0xffff0000, v166
	v_lshlrev_b32_e32 v124, 16, v164
	v_and_b32_e32 v125, 0xffff0000, v164
	v_lshlrev_b32_e32 v126, 16, v165
	v_and_b32_e32 v127, 0xffff0000, v165
	v_lshlrev_b32_e32 v130, 16, v167
	v_and_b32_e32 v131, 0xffff0000, v167
	v_pk_fma_f32 v[122:123], v[122:123], v[38:39], v[126:127]
	v_pk_fma_f32 v[120:121], v[120:121], v[36:37], v[124:125]
	v_pk_fma_f32 v[124:125], v[118:119], v[30:31], v[130:131]
	v_pk_fma_f32 v[118:119], v[116:117], v[28:29], v[128:129]
	v_cvt_pk_bf16_f32 v116, v120, v121
	v_cvt_pk_bf16_f32 v117, v122, v123
	v_cvt_pk_bf16_f32 v118, v118, v119
	v_cvt_pk_bf16_f32 v119, v124, v125
	global_store_dwordx4 v[172:173], v[116:119], off offset:256
	s_waitcnt vmcnt(12)
	v_lshlrev_b32_e32 v120, 16, v162
	v_lshlrev_b32_e32 v116, 16, v160
	v_and_b32_e32 v117, 0xffff0000, v160
	v_lshlrev_b32_e32 v118, 16, v161
	v_and_b32_e32 v119, 0xffff0000, v161
	v_and_b32_e32 v121, 0xffff0000, v162
	v_lshlrev_b32_e32 v122, 16, v163
	v_and_b32_e32 v123, 0xffff0000, v163
	v_pk_fma_f32 v[100:101], v[100:101], v[46:47], v[118:119]
	v_pk_fma_f32 v[98:99], v[98:99], v[44:45], v[116:117]
	v_pk_fma_f32 v[104:105], v[104:105], v[42:43], v[122:123]
	v_pk_fma_f32 v[102:103], v[102:103], v[40:41], v[120:121]
	v_cvt_pk_bf16_f32 v98, v98, v99
	v_cvt_pk_bf16_f32 v99, v100, v101
	v_cvt_pk_bf16_f32 v100, v102, v103
	v_cvt_pk_bf16_f32 v101, v104, v105
	global_store_dwordx4 v[170:171], v[98:101], off
	v_lshlrev_b32_e32 v102, 16, v154
	v_and_b32_e32 v103, 0xffff0000, v154
	v_lshlrev_b32_e32 v98, 16, v152
	v_and_b32_e32 v99, 0xffff0000, v152
	v_lshlrev_b32_e32 v100, 16, v153
	v_and_b32_e32 v101, 0xffff0000, v153
	v_lshlrev_b32_e32 v104, 16, v155
	v_and_b32_e32 v105, 0xffff0000, v155
	v_pk_fma_f32 v[100:101], v[108:109], v[38:39], v[100:101]
	v_pk_fma_f32 v[98:99], v[106:107], v[36:37], v[98:99]
	v_pk_fma_f32 v[104:105], v[112:113], v[30:31], v[104:105]
	v_pk_fma_f32 v[102:103], v[110:111], v[28:29], v[102:103]
	v_cvt_pk_bf16_f32 v98, v98, v99
	v_cvt_pk_bf16_f32 v99, v100, v101
	v_cvt_pk_bf16_f32 v100, v102, v103
	v_cvt_pk_bf16_f32 v101, v104, v105
	global_store_dwordx4 v[170:171], v[98:101], off offset:256
	v_lshlrev_b32_e32 v102, 16, v158
	v_and_b32_e32 v103, 0xffff0000, v158
	v_lshlrev_b32_e32 v98, 16, v156
	v_and_b32_e32 v99, 0xffff0000, v156
	v_lshlrev_b32_e32 v100, 16, v157
	v_and_b32_e32 v101, 0xffff0000, v157
	v_lshlrev_b32_e32 v104, 16, v159
	v_and_b32_e32 v105, 0xffff0000, v159
	v_pk_fma_f32 v[84:85], v[84:85], v[46:47], v[100:101]
	v_pk_fma_f32 v[82:83], v[82:83], v[44:45], v[98:99]
	v_pk_fma_f32 v[88:89], v[88:89], v[42:43], v[104:105]
	v_pk_fma_f32 v[86:87], v[86:87], v[40:41], v[102:103]
	v_cvt_pk_bf16_f32 v82, v82, v83
	v_cvt_pk_bf16_f32 v83, v84, v85
	v_cvt_pk_bf16_f32 v84, v86, v87
	v_cvt_pk_bf16_f32 v85, v88, v89
	global_store_dwordx4 v[168:169], v[82:85], off
	v_lshlrev_b32_e32 v86, 16, v150
	v_and_b32_e32 v87, 0xffff0000, v150
	v_lshlrev_b32_e32 v82, 16, v148
	v_and_b32_e32 v83, 0xffff0000, v148
	v_lshlrev_b32_e32 v84, 16, v149
	v_and_b32_e32 v85, 0xffff0000, v149
	v_lshlrev_b32_e32 v88, 16, v151
	v_and_b32_e32 v89, 0xffff0000, v151
	v_pk_fma_f32 v[84:85], v[92:93], v[38:39], v[84:85]
	v_pk_fma_f32 v[82:83], v[90:91], v[36:37], v[82:83]
	v_pk_fma_f32 v[88:89], v[96:97], v[30:31], v[88:89]
	v_pk_fma_f32 v[86:87], v[94:95], v[28:29], v[86:87]
	v_cvt_pk_bf16_f32 v82, v82, v83
	v_cvt_pk_bf16_f32 v83, v84, v85
	v_cvt_pk_bf16_f32 v84, v86, v87
	v_cvt_pk_bf16_f32 v85, v88, v89
	v_add_co_u32_e32 v86, vcc, s2, v188
	global_store_dwordx4 v[168:169], v[82:85], off offset:256
	s_nop 0
	v_addc_co_u32_e32 v87, vcc, 0, v189, vcc
	s_mov_b32 s2, 0x48000
	v_add_co_u32_e32 v88, vcc, s2, v188
	s_mov_b32 s2, 0x50000
	s_nop 0
	v_addc_co_u32_e32 v89, vcc, 0, v189, vcc
	v_add_co_u32_e32 v112, vcc, s2, v188
	s_mov_b32 s2, 0x58000
	s_nop 0
	v_addc_co_u32_e32 v113, vcc, 0, v189, vcc
	v_add_co_u32_e32 v90, vcc, s2, v188
	s_waitcnt vmcnt(10)
	v_lshlrev_b32_e32 v124, 16, v194
	v_addc_co_u32_e32 v91, vcc, 0, v189, vcc
	v_and_b32_e32 v125, 0xffff0000, v194
	v_lshlrev_b32_e32 v82, 16, v195
	v_and_b32_e32 v83, 0xffff0000, v195
	v_lshlrev_b32_e32 v126, 16, v196
	v_and_b32_e32 v127, 0xffff0000, v196
	v_lshlrev_b32_e32 v84, 16, v197
	v_and_b32_e32 v85, 0xffff0000, v197
	v_pk_fma_f32 v[80:81], v[80:81], v[46:47], v[82:83]
	v_pk_fma_f32 v[78:79], v[78:79], v[44:45], v[124:125]
	v_pk_fma_f32 v[82:83], v[76:77], v[42:43], v[84:85]
	v_pk_fma_f32 v[76:77], v[74:75], v[40:41], v[126:127]
	v_cvt_pk_bf16_f32 v74, v78, v79
	v_cvt_pk_bf16_f32 v75, v80, v81
	v_cvt_pk_bf16_f32 v76, v76, v77
	v_cvt_pk_bf16_f32 v77, v82, v83
	global_store_dwordx4 v[86:87], v[74:77], off
	v_lshlrev_b32_e32 v78, 16, v200
	v_and_b32_e32 v79, 0xffff0000, v200
	v_lshlrev_b32_e32 v74, 16, v198
	v_and_b32_e32 v75, 0xffff0000, v198
	v_lshlrev_b32_e32 v76, 16, v199
	v_and_b32_e32 v77, 0xffff0000, v199
	v_lshlrev_b32_e32 v80, 16, v201
	v_and_b32_e32 v81, 0xffff0000, v201
	v_pk_fma_f32 v[72:73], v[72:73], v[38:39], v[76:77]
	v_pk_fma_f32 v[70:71], v[70:71], v[36:37], v[74:75]
	v_pk_fma_f32 v[74:75], v[68:69], v[30:31], v[80:81]
	v_pk_fma_f32 v[68:69], v[66:67], v[28:29], v[78:79]
	v_cvt_pk_bf16_f32 v66, v70, v71
	v_cvt_pk_bf16_f32 v67, v72, v73
	v_cvt_pk_bf16_f32 v68, v68, v69
	v_cvt_pk_bf16_f32 v69, v74, v75
	global_store_dwordx4 v[86:87], v[66:69], off offset:256
	v_lshlrev_b32_e32 v70, 16, v208
	v_and_b32_e32 v71, 0xffff0000, v208
	v_lshlrev_b32_e32 v66, 16, v206
	v_and_b32_e32 v67, 0xffff0000, v206
	v_lshlrev_b32_e32 v68, 16, v207
	v_and_b32_e32 v69, 0xffff0000, v207
	v_lshlrev_b32_e32 v72, 16, v209
	v_and_b32_e32 v73, 0xffff0000, v209
	v_pk_fma_f32 v[62:63], v[62:63], v[46:47], v[68:69]
	v_pk_fma_f32 v[60:61], v[60:61], v[44:45], v[66:67]
	v_pk_fma_f32 v[66:67], v[58:59], v[42:43], v[72:73]
	v_pk_fma_f32 v[58:59], v[56:57], v[40:41], v[70:71]
	v_cvt_pk_bf16_f32 v56, v60, v61
	v_cvt_pk_bf16_f32 v57, v62, v63
	v_cvt_pk_bf16_f32 v58, v58, v59
	v_cvt_pk_bf16_f32 v59, v66, v67
	global_store_dwordx4 v[88:89], v[56:59], off
	v_lshlrev_b32_e32 v60, 16, v212
	v_and_b32_e32 v61, 0xffff0000, v212
	v_lshlrev_b32_e32 v56, 16, v210
	v_and_b32_e32 v57, 0xffff0000, v210
	v_lshlrev_b32_e32 v58, 16, v211
	v_and_b32_e32 v59, 0xffff0000, v211
	v_lshlrev_b32_e32 v62, 16, v213
	v_and_b32_e32 v63, 0xffff0000, v213
	v_pk_fma_f32 v[54:55], v[54:55], v[38:39], v[58:59]
	v_pk_fma_f32 v[52:53], v[52:53], v[36:37], v[56:57]
	v_pk_fma_f32 v[56:57], v[50:51], v[30:31], v[62:63]
	v_pk_fma_f32 v[50:51], v[48:49], v[28:29], v[60:61]
	v_cvt_pk_bf16_f32 v48, v52, v53
	v_cvt_pk_bf16_f32 v49, v54, v55
	v_cvt_pk_bf16_f32 v50, v50, v51
	v_cvt_pk_bf16_f32 v51, v56, v57
	global_store_dwordx4 v[88:89], v[48:51], off offset:256
	v_lshlrev_b32_e32 v52, 16, v216
	v_and_b32_e32 v53, 0xffff0000, v216
	v_lshlrev_b32_e32 v48, 16, v214
	v_and_b32_e32 v49, 0xffff0000, v214
	v_lshlrev_b32_e32 v50, 16, v215
	v_and_b32_e32 v51, 0xffff0000, v215
	v_lshlrev_b32_e32 v54, 16, v217
	v_and_b32_e32 v55, 0xffff0000, v217
	v_pk_fma_f32 v[34:35], v[34:35], v[46:47], v[50:51]
	v_pk_fma_f32 v[32:33], v[32:33], v[44:45], v[48:49]
	v_pk_fma_f32 v[48:49], v[26:27], v[42:43], v[54:55]
	v_pk_fma_f32 v[26:27], v[24:25], v[40:41], v[52:53]
	v_cvt_pk_bf16_f32 v24, v32, v33
	v_cvt_pk_bf16_f32 v25, v34, v35
	v_cvt_pk_bf16_f32 v26, v26, v27
	v_cvt_pk_bf16_f32 v27, v48, v49
	global_store_dwordx4 v[112:113], v[24:27], off
	v_lshlrev_b32_e32 v32, 16, v220
	v_and_b32_e32 v33, 0xffff0000, v220
	v_lshlrev_b32_e32 v24, 16, v218
	v_and_b32_e32 v25, 0xffff0000, v218
	v_lshlrev_b32_e32 v26, 16, v219
	v_and_b32_e32 v27, 0xffff0000, v219
	v_lshlrev_b32_e32 v34, 16, v221
	v_and_b32_e32 v35, 0xffff0000, v221
	v_pk_fma_f32 v[22:23], v[22:23], v[38:39], v[26:27]
	v_pk_fma_f32 v[20:21], v[20:21], v[36:37], v[24:25]
	v_pk_fma_f32 v[24:25], v[18:19], v[30:31], v[34:35]
	v_pk_fma_f32 v[18:19], v[16:17], v[28:29], v[32:33]
	v_cvt_pk_bf16_f32 v16, v20, v21
	v_cvt_pk_bf16_f32 v17, v22, v23
	v_cvt_pk_bf16_f32 v18, v18, v19
	v_cvt_pk_bf16_f32 v19, v24, v25
	global_store_dwordx4 v[112:113], v[16:19], off offset:256
	s_waitcnt vmcnt(14)
	v_lshlrev_b32_e32 v20, 16, v224
	v_and_b32_e32 v21, 0xffff0000, v224
	v_lshlrev_b32_e32 v16, 16, v222
	v_and_b32_e32 v17, 0xffff0000, v222
	v_lshlrev_b32_e32 v18, 16, v223
	v_and_b32_e32 v19, 0xffff0000, v223
	v_lshlrev_b32_e32 v22, 16, v225
	v_and_b32_e32 v23, 0xffff0000, v225
	v_pk_fma_f32 v[14:15], v[14:15], v[46:47], v[18:19]
	v_pk_fma_f32 v[12:13], v[12:13], v[44:45], v[16:17]
	v_pk_fma_f32 v[16:17], v[10:11], v[42:43], v[22:23]
	v_pk_fma_f32 v[10:11], v[8:9], v[40:41], v[20:21]
	v_cvt_pk_bf16_f32 v8, v12, v13
	v_cvt_pk_bf16_f32 v9, v14, v15
	v_cvt_pk_bf16_f32 v10, v10, v11
	v_cvt_pk_bf16_f32 v11, v16, v17
	global_store_dwordx4 v[90:91], v[8:11], off
	v_lshlrev_b32_e32 v12, 16, v228
	v_and_b32_e32 v13, 0xffff0000, v228
	v_lshlrev_b32_e32 v8, 16, v226
	v_and_b32_e32 v9, 0xffff0000, v226
	v_lshlrev_b32_e32 v10, 16, v227
	v_and_b32_e32 v11, 0xffff0000, v227
	v_lshlrev_b32_e32 v14, 16, v229
	v_and_b32_e32 v15, 0xffff0000, v229
	v_pk_fma_f32 v[6:7], v[6:7], v[38:39], v[10:11]
	v_pk_fma_f32 v[4:5], v[4:5], v[36:37], v[8:9]
	v_pk_fma_f32 v[8:9], v[2:3], v[30:31], v[14:15]
	v_pk_fma_f32 v[2:3], v[0:1], v[28:29], v[12:13]
	v_cvt_pk_bf16_f32 v0, v4, v5
	v_cvt_pk_bf16_f32 v1, v6, v7
	v_cvt_pk_bf16_f32 v2, v2, v3
	v_cvt_pk_bf16_f32 v3, v8, v9
	global_store_dwordx4 v[90:91], v[0:3], off offset:256
	s_andn2_b64 vcc, exec, s[0:1]
	s_mov_b64 s[0:1], -1
	s_cbranch_vccnz .LBB0_1107
